# speedup vs baseline: 1.0471x; 1.0117x over previous
.Lcsr_sc_done:
	s_waitcnt lgkmcnt(0)
	s_barrier
	v_and_b32_e32 v4, 7, v88
	v_lshlrev_b32_e32 v4, 6, v4
	v_add_u32_e32 v4, 0x8f20, v4
	ds_read2_b32 v[4:5], v4 offset1:16
	s_waitcnt lgkmcnt(0)
	v_sub_u32_e32 v5, v5, v4
	v_cmp_lt_u32_e32 vcc, 0x400, v5
	s_cmp_eq_u64 vcc, 0
	s_cselect_b32 s34, 1, 0
	s_and_saveexec_b64 s[20:21], s[6:7]
	s_cbranch_execz .Lcsr_rows_done
	v_and_b32_e32 v9, 0x1c0, v3
	ds_read_b32 v9, v9 offset:36640
	v_lshrrev_b32_e32 v10, 4, v0
	v_lshlrev_b32_e32 v10, 10, v10
	s_cmp_eq_u32 s34, 1
	s_cselect_b64 s[24:25], -1, 0
	v_mov_b32_e32 v1, 0x8f20
	v_lshl_add_u32 v1, v0, 2, v1
	ds_read2_b32 v[6:7], v1 offset1:1
	ds_read_b32 v8, v3 offset:38192
	v_lshl_or_b32 v4, s2, 7, v0
	s_mov_b32 s22, 0xc350
	v_cmp_gt_u32_e32 vcc, s22, v4
	s_waitcnt lgkmcnt(0)
	v_add_f32_e32 v1, 1.0, v8
	v_sub_u32_e32 v10, v10, v9
	v_cndmask_b32_e64 v10, 0, v10, s[24:25]
	v_add_u32_e32 v6, v6, v10
	v_add_u32_e32 v7, v7, v10
	s_and_b64 exec, exec, vcc
	s_cbranch_execz .Lcsr_rows_done
	v_mov_b32_e32 v5, 0
	v_lshlrev_b64 v[8:9], 2, v[4:5]
	v_add_u32_e32 v3, v6, v2
	v_lshl_add_u64 v[10:11], s[60:61], 0, v[8:9]
	global_store_dword v[10:11], v3, off
	v_add_u32_e32 v3, v7, v2
	v_lshl_add_u64 v[6:7], s[62:63], 0, v[8:9]
	global_store_dword v[6:7], v3, off
	v_cmp_lt_f32_e32 vcc, 0, v1
	v_mov_b32_e32 v3, v5
	s_and_saveexec_b64 s[22:23], vcc
	s_cbranch_execz .Lcsr_dinv_done
	s_mov_b32 s26, 0xf800000
	v_mul_f32_e32 v3, 0x4f800000, v1
	v_cmp_gt_f32_e32 vcc, s26, v1
	s_nop 1
	v_cndmask_b32_e32 v1, v1, v3, vcc
	v_sqrt_f32_e32 v3, v1
	s_nop 0
	v_add_u32_e32 v6, -1, v3
	v_fma_f32 v7, -v6, v3, v1
	v_cmp_ge_f32_e64 s[24:25], 0, v7
	v_add_u32_e32 v7, 1, v3
	s_nop 0
	v_cndmask_b32_e64 v6, v3, v6, s[24:25]
	v_fma_f32 v3, -v7, v3, v1
	v_cmp_lt_f32_e64 s[24:25], 0, v3
	s_nop 1
	v_cndmask_b32_e64 v3, v6, v7, s[24:25]
	v_mul_f32_e32 v6, 0x37800000, v3
	v_cndmask_b32_e32 v3, v3, v6, vcc
	v_mov_b32_e32 v6, 0x260
	v_cmp_class_f32_e32 vcc, v1, v6
	s_nop 1
	v_cndmask_b32_e32 v1, v3, v1, vcc
	v_div_scale_f32 v3, s[24:25], v1, v1, 1.0
	v_rcp_f32_e32 v6, v3
	s_nop 0
	v_fma_f32 v7, -v3, v6, 1.0
	v_fmac_f32_e32 v6, v7, v6
	v_div_scale_f32 v7, vcc, 1.0, v1, 1.0
	v_mul_f32_e32 v8, v7, v6
	v_fma_f32 v9, -v3, v8, v7
	v_fmac_f32_e32 v8, v9, v6
	v_fma_f32 v3, -v3, v8, v7
	v_div_fmas_f32 v3, v3, v6, v8
	v_div_fixup_f32 v3, v3, v1, 1.0

.Lcsr_rows_done:
	s_mov_b64 exec, -1
	s_cmp_eq_u32 s34, 1
	s_cbranch_scc0 .Lcsr_dense
	s_mov_b32 s35, 0
.Lcsr_tile_loop:
	s_lshl_b32 s36, s35, 6
	v_mov_b32_e32 v4, s36
	v_add_u32_e32 v4, 0x8f20, v4
	ds_read2_b32 v[4:5], v4 offset1:16
	s_lshl_b32 s39, s35, 10
	s_waitcnt lgkmcnt(0)
	v_readfirstlane_b32 s37, v4
	v_readfirstlane_b32 s38, v5
	s_sub_i32 s38, s38, s37
	s_cmpk_lt_i32 s38, 0x1
	s_cbranch_scc1 .Lcsr_next_tile
	v_mov_b32_e32 v6, v0
	v_cmp_gt_i32_e64 s[20:21], s38, v6
	v_add_u32_e32 v7, s37, v6
	v_lshlrev_b32_e32 v7, 3, v7
	v_add3_u32 v10, v2, s39, v6
	v_mov_b32_e32 v11, 0
	v_lshl_add_u64 v[10:11], v[10:11], 3, s[54:55]
	s_and_saveexec_b64 s[22:23], s[20:21]
	s_cbranch_execz .Lcsr_ts_skip0
	ds_read_b64 v[8:9], v7
	s_waitcnt lgkmcnt(0)
	global_store_dwordx2 v[10:11], v[8:9], off sc1
.Lcsr_ts_skip0:
	s_mov_b64 exec, s[22:23]
	s_cmpk_lt_i32 s38, 0x101
	s_cbranch_scc1 .Lcsr_next_tile
	v_add_u32_e32 v6, 0x100, v0
	v_cmp_gt_i32_e64 s[20:21], s38, v6
	v_add_u32_e32 v7, s37, v6
	v_lshlrev_b32_e32 v7, 3, v7
	v_add3_u32 v10, v2, s39, v6
	v_mov_b32_e32 v11, 0
	v_lshl_add_u64 v[10:11], v[10:11], 3, s[54:55]
	s_and_saveexec_b64 s[22:23], s[20:21]
	s_cbranch_execz .Lcsr_ts_skip1
	ds_read_b64 v[8:9], v7
	s_waitcnt lgkmcnt(0)
	global_store_dwordx2 v[10:11], v[8:9], off sc1
.Lcsr_ts_skip1:
	s_mov_b64 exec, s[22:23]
	s_cmpk_lt_i32 s38, 0x201
	s_cbranch_scc1 .Lcsr_next_tile
	v_add_u32_e32 v6, 0x200, v0
	v_cmp_gt_i32_e64 s[20:21], s38, v6
	v_add_u32_e32 v7, s37, v6
	v_lshlrev_b32_e32 v7, 3, v7
	v_add3_u32 v10, v2, s39, v6
	v_mov_b32_e32 v11, 0
	v_lshl_add_u64 v[10:11], v[10:11], 3, s[54:55]
	s_and_saveexec_b64 s[22:23], s[20:21]
	s_cbranch_execz .Lcsr_ts_skip2
	ds_read_b64 v[8:9], v7
	s_waitcnt lgkmcnt(0)
	global_store_dwordx2 v[10:11], v[8:9], off sc1
.Lcsr_ts_skip2:
	s_mov_b64 exec, s[22:23]
	s_cmpk_lt_i32 s38, 0x301
	s_cbranch_scc1 .Lcsr_next_tile
	v_add_u32_e32 v6, 0x300, v0
	v_cmp_gt_i32_e64 s[20:21], s38, v6
	v_add_u32_e32 v7, s37, v6
	v_lshlrev_b32_e32 v7, 3, v7
	v_add3_u32 v10, v2, s39, v6
	v_mov_b32_e32 v11, 0
	v_lshl_add_u64 v[10:11], v[10:11], 3, s[54:55]
	s_and_saveexec_b64 s[22:23], s[20:21]
	s_cbranch_execz .Lcsr_ts_skip3
	ds_read_b64 v[8:9], v7
	s_waitcnt lgkmcnt(0)
	global_store_dwordx2 v[10:11], v[8:9], off sc1

.Lcsr_next_tile:
	s_add_i32 s35, s35, 1
	s_cmp_lt_i32 s35, 8
	s_cbranch_scc1 .Lcsr_tile_loop
	s_endpgm
.Lcsr_dense:
	s_cmpk_lt_i32 s33, 0x1
	s_cbranch_scc1 .Lcsr_st_done
	v_mov_b32_e32 v12, v0
	v_cmp_gt_i32_e64 s[20:21], s33, v12
	v_lshlrev_b32_e32 v4, 3, v12
	v_add_u32_e32 v14, 0x100, v0
	v_cmp_gt_i32_e64 s[22:23], s33, v14
	v_lshlrev_b32_e32 v6, 3, v14
	v_add_u32_e32 v16, 0x200, v0
	v_cmp_gt_i32_e64 s[24:25], s33, v16
	v_lshlrev_b32_e32 v8, 3, v16
	v_add_u32_e32 v18, 0x300, v0
	v_cmp_gt_i32_e64 s[26:27], s33, v18
	v_lshlrev_b32_e32 v10, 3, v18
	s_mov_b64 exec, s[20:21]
	ds_read_b64 v[4:5], v4
	s_mov_b64 exec, s[22:23]
	ds_read_b64 v[6:7], v6
	s_mov_b64 exec, s[24:25]
	ds_read_b64 v[8:9], v8
	s_mov_b64 exec, s[26:27]
	ds_read_b64 v[10:11], v10
	s_mov_b64 exec, -1
	v_add_u32_e32 v12, v12, v2
	v_mov_b32_e32 v13, 0
	v_lshl_add_u64 v[12:13], v[12:13], 3, s[54:55]
	v_add_u32_e32 v14, v14, v2
	v_mov_b32_e32 v15, 0
	v_lshl_add_u64 v[14:15], v[14:15], 3, s[54:55]
	v_add_u32_e32 v16, v16, v2
	v_mov_b32_e32 v17, 0
	v_lshl_add_u64 v[16:17], v[16:17], 3, s[54:55]
	v_add_u32_e32 v18, v18, v2
	v_mov_b32_e32 v19, 0
	v_lshl_add_u64 v[18:19], v[18:19], 3, s[54:55]
	s_mov_b64 exec, s[20:21]
	s_cbranch_execz .Lcsr_st_skip0
	s_waitcnt lgkmcnt(3)
	global_store_dwordx2 v[12:13], v[4:5], off sc1

_Z5k_aggILb0ELi4ELb1EEvPK15HIP_vector_typeIjLj4EEPKS0_IiLj2EEPKiS8_PKfSA_PKDv8_DF16_PDF16_Pf:
	s_lshl_b32 s69, s2, 10
	v_cmp_gt_u32_e32 vcc, 16, v0
	s_and_saveexec_b64 s[4:5], vcc
	v_lshlrev_b32_e32 v1, 2, v0
	v_mov_b32_e32 v2, -1
	ds_write_b32 v1, v2 offset:17408
	s_or_b64 exec, exec, s[4:5]
	s_load_dwordx8 s[36:43], s[0:1], 0x0
	s_load_dwordx4 s[44:47], s[0:1], 0x20
	s_load_dwordx2 s[50:51], s[0:1], 0x30
	s_movk_i32 s3, 0x110
	v_cmp_gt_u32_e64 s[4:5], s3, v0
	v_lshlrev_b32_e32 v22, 4, v0
	s_and_saveexec_b64 s[6:7], s[4:5]
	s_cbranch_execz .LBB2_5
	v_mov_b32_e32 v2, 0
	v_or_b32_e32 v1, 0xffffff00, v0
	s_mov_b64 s[8:9], 0
	v_mov_b32_e32 v3, v2
	v_mov_b32_e32 v4, v2
	v_mov_b32_e32 v5, v2
	v_mov_b32_e32 v6, v22

.LBB2_5:
	s_or_b64 exec, exec, s[6:7]
	s_lshl_b32 s52, s2, 4
	s_ashr_i32 s53, s52, 31
	s_load_dwordx2 s[48:49], s[0:1], 0x38
	s_lshl_b64 s[0:1], s[52:53], 2
	s_waitcnt lgkmcnt(0)
	v_add_u32_e32 v8, s69, v0
	v_mov_b32_e32 v9, 0
	v_lshl_add_u64 v[8:9], v[8:9], 3, s[38:39]
	v_cmp_gt_u32_e64 s[6:7], 64, v0
	s_and_saveexec_b64 s[4:5], s[6:7]
	s_cbranch_execz .Lagg2_nospecb
	global_load_dwordx2 v[10:11], v[8:9], off offset:2048
.Lagg2_nospecb:
	s_mov_b64 exec, s[4:5]
	global_load_dwordx2 v[8:9], v[8:9], off
	s_add_u32 s0, s40, s0
	s_addc_u32 s1, s41, s1
	s_load_dword s33, s[0:1], 0x0
	s_min_i32 s0, s52, 0xc340
	s_ashr_i32 s1, s0, 31
	s_lshl_b64 s[0:1], s[0:1], 2
	s_add_u32 s0, s42, s0
	s_addc_u32 s1, s43, s1
	s_load_dword s53, s[0:1], 0x3c
	v_and_b32_e32 v1, 15, v0
	v_lshrrev_b32_e32 v23, 4, v0
	v_lshlrev_b32_e32 v24, 4, v1
	s_waitcnt lgkmcnt(0)
	s_cmp_ge_i32 s33, s53
	s_barrier
	s_cbranch_scc1 .Lagg2_empty
	v_mov_b32_e32 v2, 0x4400
	v_lshl_or_b32 v42, v0, 2, v2
	v_lshl_or_b32 v43, v23, 2, v2
	v_mov_b32_e32 v2, 0x2200
	v_or_b32_e32 v25, 0x3400, v24
	v_cmp_eq_u32_e64 s[0:1], 0, v1
	v_cmp_eq_u32_e64 s[2:3], 1, v23
	v_cmp_eq_u32_e64 s[4:5], 2, v23
	v_cmp_eq_u32_e64 s[6:7], 3, v23
	v_cmp_eq_u32_e64 s[8:9], 4, v23
	v_cmp_eq_u32_e64 s[10:11], 5, v23
	v_cmp_eq_u32_e64 s[12:13], 6, v23
	v_cmp_eq_u32_e64 s[14:15], 7, v23
	v_cmp_eq_u32_e64 s[16:17], 8, v23
	v_cmp_eq_u32_e64 s[18:19], 9, v23
	v_cmp_eq_u32_e64 s[20:21], 10, v23
	v_cmp_eq_u32_e64 s[22:23], 11, v23
	v_cmp_eq_u32_e64 s[24:25], 12, v23
	v_cmp_eq_u32_e64 s[26:27], 13, v23
	v_cmp_eq_u32_e64 s[28:29], 14, v23
	v_cmp_eq_u32_e64 s[30:31], 15, v23
	v_add_u32_e32 v26, s33, v0
	v_lshl_add_u32 v44, v0, 3, v2
	v_mov_b32_e32 v45, 0
	s_movk_i32 s66, 0x110
	v_mov_b32_e32 v46, -1
	s_mov_b64 s[40:41], 0x800
	s_mov_b32 s67, 0xffff0
	v_mov_b32_e32 v47, 2
	s_mov_b32 s68, s33
	s_branch .LBB2_8

.LBB2_44:
	s_sub_i32 s34, s53, s68
	s_min_i32 s56, s34, 0x240
	s_cmp_eq_u32 s68, s33
	s_cbranch_scc0 .Lagg2_slow
	s_cmp_eq_u32 s33, s69
	s_cbranch_scc0 .Lagg2_slow
	s_waitcnt vmcnt(0)
	v_cmp_gt_i32_e64 s[34:35], s56, v0
	s_and_saveexec_b64 s[42:43], s[34:35]
	ds_write_b64 v44, v[8:9]
	s_mov_b64 exec, s[42:43]
	v_add_u32_e32 v2, 0x100, v0
	v_cmp_gt_i32_e64 s[34:35], s56, v2
	v_cmp_gt_u32_e64 s[62:63], 64, v0
	s_and_b64 s[34:35], s[34:35], s[62:63]
	s_and_saveexec_b64 s[42:43], s[34:35]
	ds_write_b64 v44, v[10:11] offset:2048
	s_mov_b64 exec, s[42:43]
	s_cmpk_lt_i32 s56, 0x141
	s_cbranch_scc1 .LBB2_47
	v_add_u32_e32 v2, 0x140, v0
	v_cmp_gt_i32_e64 s[34:35], s56, v2
	s_and_saveexec_b64 s[42:43], s[34:35]
	s_cbranch_execz .LBB2_47
	v_add_u32_e32 v2, 0x140, v26
	v_mov_b32_e32 v3, 0
	v_lshl_add_u64 v[2:3], v[2:3], 3, s[38:39]
	global_load_dwordx2 v[6:7], v[2:3], off
	s_waitcnt vmcnt(0)
	ds_write_b64 v44, v[6:7] offset:2560
	s_branch .LBB2_47
.Lagg2_slow:
	s_waitcnt vmcnt(0)
	v_cmp_gt_i32_e64 s[34:35], s56, v0
	s_and_saveexec_b64 s[42:43], s[34:35]
	s_cbranch_execz .LBB2_47
	v_ashrrev_i32_e32 v27, 31, v26
	v_lshl_add_u64 v[2:3], v[26:27], 3, s[38:39]
	s_mov_b64 s[54:55], 0
	v_mov_b32_e32 v4, v44
	v_mov_b32_e32 v5, v0

.Lagg2_empty:
	s_waitcnt vmcnt(0)

	.amdhsa_kernel _Z5k_aggILb0ELi4ELb1EEvPK15HIP_vector_typeIjLj4EEPKS0_IiLj2EEPKiS8_PKfSA_PKDv8_DF16_PDF16_Pf
		.amdhsa_group_segment_fixed_size 17472
		.amdhsa_private_segment_fixed_size 0
		.amdhsa_kernarg_size 72
		.amdhsa_user_sgpr_count 2
		.amdhsa_user_sgpr_dispatch_ptr 0
		.amdhsa_user_sgpr_queue_ptr 0
		.amdhsa_user_sgpr_kernarg_segment_ptr 1
		.amdhsa_user_sgpr_dispatch_id 0
		.amdhsa_user_sgpr_kernarg_preload_length 0
		.amdhsa_user_sgpr_kernarg_preload_offset 0
		.amdhsa_user_sgpr_private_segment_size 0
		.amdhsa_uses_dynamic_stack 0
		.amdhsa_enable_private_segment 0
		.amdhsa_system_sgpr_workgroup_id_x 1
		.amdhsa_system_sgpr_workgroup_id_y 0
		.amdhsa_system_sgpr_workgroup_id_z 0
		.amdhsa_system_sgpr_workgroup_info 0
		.amdhsa_system_vgpr_workitem_id 0
		.amdhsa_next_free_vgpr 64
		.amdhsa_next_free_sgpr 70
		.amdhsa_accum_offset 64
		.amdhsa_reserve_vcc 1
		.amdhsa_float_round_mode_32 0
		.amdhsa_float_round_mode_16_64 0
		.amdhsa_float_denorm_mode_32 3
		.amdhsa_float_denorm_mode_16_64 3
		.amdhsa_dx10_clamp 1
		.amdhsa_ieee_mode 1
		.amdhsa_fp16_overflow 0
		.amdhsa_tg_split 0
		.amdhsa_exception_fp_ieee_invalid_op 0
		.amdhsa_exception_fp_denorm_src 0
		.amdhsa_exception_fp_ieee_div_zero 0
		.amdhsa_exception_fp_ieee_overflow 0
		.amdhsa_exception_fp_ieee_underflow 0
		.amdhsa_exception_fp_ieee_inexact 0
		.amdhsa_exception_int_div_zero 0
	.end_amdhsa_kernel

_Z5k_aggILb0ELi4ELb0EEvPK15HIP_vector_typeIjLj4EEPKS0_IiLj2EEPKiS8_PKfSA_PKDv8_DF16_PDF16_Pf:
	s_lshl_b32 s69, s2, 10
	v_cmp_gt_u32_e32 vcc, 16, v0
	s_and_saveexec_b64 s[4:5], vcc
	v_lshlrev_b32_e32 v1, 2, v0
	v_mov_b32_e32 v2, -1
	ds_write_b32 v1, v2 offset:17408
	s_or_b64 exec, exec, s[4:5]
	s_load_dwordx8 s[36:43], s[0:1], 0x0
	s_load_dwordx4 s[44:47], s[0:1], 0x20
	s_load_dwordx2 s[50:51], s[0:1], 0x30
	s_movk_i32 s3, 0x110
	v_cmp_gt_u32_e64 s[4:5], s3, v0
	v_lshlrev_b32_e32 v18, 4, v0
	s_and_saveexec_b64 s[6:7], s[4:5]
	s_cbranch_execz .LBB3_5
	v_mov_b32_e32 v2, 0
	v_or_b32_e32 v1, 0xffffff00, v0
	s_mov_b64 s[8:9], 0
	v_mov_b32_e32 v3, v2
	v_mov_b32_e32 v4, v2
	v_mov_b32_e32 v5, v2
	v_mov_b32_e32 v6, v18

.Lagg3_nospecb:
	s_mov_b64 exec, s[4:5]
	global_load_dwordx2 v[8:9], v[8:9], off
	s_add_u32 s0, s40, s0
	s_addc_u32 s1, s41, s1
	s_load_dword s33, s[0:1], 0x0
	s_min_i32 s0, s52, 0xc340
	s_ashr_i32 s1, s0, 31
	s_lshl_b64 s[0:1], s[0:1], 2
	s_add_u32 s0, s42, s0
	s_addc_u32 s1, s43, s1
	s_load_dword s53, s[0:1], 0x3c
	v_and_b32_e32 v1, 15, v0
	v_lshrrev_b32_e32 v19, 4, v0
	v_lshlrev_b32_e32 v20, 4, v1
	s_waitcnt lgkmcnt(0)
	s_cmp_ge_i32 s33, s53
	s_barrier
	s_cbranch_scc1 .Lagg3_empty
	v_mov_b32_e32 v2, 0x4400
	v_lshl_or_b32 v40, v0, 2, v2
	v_lshl_or_b32 v41, v19, 2, v2
	v_mov_b32_e32 v2, 0x2200
	v_or_b32_e32 v21, 0x3400, v20
	v_cmp_eq_u32_e64 s[0:1], 0, v1
	v_cmp_eq_u32_e64 s[2:3], 1, v19
	v_cmp_eq_u32_e64 s[4:5], 2, v19
	v_cmp_eq_u32_e64 s[6:7], 3, v19
	v_cmp_eq_u32_e64 s[8:9], 4, v19
	v_cmp_eq_u32_e64 s[10:11], 5, v19
	v_cmp_eq_u32_e64 s[12:13], 6, v19
	v_cmp_eq_u32_e64 s[14:15], 7, v19
	v_cmp_eq_u32_e64 s[16:17], 8, v19
	v_cmp_eq_u32_e64 s[18:19], 9, v19
	v_cmp_eq_u32_e64 s[20:21], 10, v19
	v_cmp_eq_u32_e64 s[22:23], 11, v19
	v_cmp_eq_u32_e64 s[24:25], 12, v19
	v_cmp_eq_u32_e64 s[26:27], 13, v19
	v_cmp_eq_u32_e64 s[28:29], 14, v19
	v_cmp_eq_u32_e64 s[30:31], 15, v19
	v_add_u32_e32 v22, s33, v0
	v_lshl_add_u32 v42, v0, 3, v2
	v_mov_b32_e32 v43, 0
	s_movk_i32 s66, 0x110
	v_mov_b32_e32 v44, -1
	s_mov_b64 s[40:41], 0x800
	s_mov_b32 s67, 0xffff0
	s_mov_b32 s68, s33
	s_branch .LBB3_8

.LBB3_44:
	s_sub_i32 s34, s53, s68
	s_min_i32 s56, s34, 0x240
	s_cmp_eq_u32 s68, s33
	s_cbranch_scc0 .Lagg3_slow
	s_cmp_eq_u32 s33, s69
	s_cbranch_scc0 .Lagg3_slow
	s_waitcnt vmcnt(0)
	v_cmp_gt_i32_e64 s[34:35], s56, v0
	s_and_saveexec_b64 s[42:43], s[34:35]
	ds_write_b64 v42, v[8:9]
	s_mov_b64 exec, s[42:43]
	v_add_u32_e32 v2, 0x100, v0
	v_cmp_gt_i32_e64 s[34:35], s56, v2
	v_cmp_gt_u32_e64 s[62:63], 64, v0
	s_and_b64 s[34:35], s[34:35], s[62:63]
	s_and_saveexec_b64 s[42:43], s[34:35]
	ds_write_b64 v42, v[10:11] offset:2048
	s_mov_b64 exec, s[42:43]
	s_cmpk_lt_i32 s56, 0x141
	s_cbranch_scc1 .LBB3_47
	v_add_u32_e32 v2, 0x140, v0
	v_cmp_gt_i32_e64 s[34:35], s56, v2
	s_and_saveexec_b64 s[42:43], s[34:35]
	s_cbranch_execz .LBB3_47
	v_add_u32_e32 v2, 0x140, v22
	v_mov_b32_e32 v3, 0
	v_lshl_add_u64 v[2:3], v[2:3], 3, s[38:39]
	global_load_dwordx2 v[6:7], v[2:3], off
	s_waitcnt vmcnt(0)
	ds_write_b64 v42, v[6:7] offset:2560
	s_branch .LBB3_47
.Lagg3_slow:
	s_waitcnt vmcnt(0)
	v_cmp_gt_i32_e64 s[34:35], s56, v0
	s_and_saveexec_b64 s[42:43], s[34:35]
	s_cbranch_execz .LBB3_47
	v_ashrrev_i32_e32 v23, 31, v22
	v_lshl_add_u64 v[2:3], v[22:23], 3, s[38:39]
	s_mov_b64 s[54:55], 0
	v_mov_b32_e32 v4, v42
	v_mov_b32_e32 v5, v0

	.amdhsa_kernel _Z5k_aggILb0ELi4ELb0EEvPK15HIP_vector_typeIjLj4EEPKS0_IiLj2EEPKiS8_PKfSA_PKDv8_DF16_PDF16_Pf
		.amdhsa_group_segment_fixed_size 17472
		.amdhsa_private_segment_fixed_size 0
		.amdhsa_kernarg_size 72
		.amdhsa_user_sgpr_count 2
		.amdhsa_user_sgpr_dispatch_ptr 0
		.amdhsa_user_sgpr_queue_ptr 0
		.amdhsa_user_sgpr_kernarg_segment_ptr 1
		.amdhsa_user_sgpr_dispatch_id 0
		.amdhsa_user_sgpr_kernarg_preload_length 0
		.amdhsa_user_sgpr_kernarg_preload_offset 0
		.amdhsa_user_sgpr_private_segment_size 0
		.amdhsa_uses_dynamic_stack 0
		.amdhsa_enable_private_segment 0
		.amdhsa_system_sgpr_workgroup_id_x 1
		.amdhsa_system_sgpr_workgroup_id_y 0
		.amdhsa_system_sgpr_workgroup_id_z 0
		.amdhsa_system_sgpr_workgroup_info 0
		.amdhsa_system_vgpr_workitem_id 0
		.amdhsa_next_free_vgpr 62
		.amdhsa_next_free_sgpr 70
		.amdhsa_accum_offset 64
		.amdhsa_reserve_vcc 1
		.amdhsa_float_round_mode_32 0
		.amdhsa_float_round_mode_16_64 0
		.amdhsa_float_denorm_mode_32 3
		.amdhsa_float_denorm_mode_16_64 3
		.amdhsa_dx10_clamp 1
		.amdhsa_ieee_mode 1
		.amdhsa_fp16_overflow 0
		.amdhsa_tg_split 0
		.amdhsa_exception_fp_ieee_invalid_op 0
		.amdhsa_exception_fp_denorm_src 0
		.amdhsa_exception_fp_ieee_div_zero 0
		.amdhsa_exception_fp_ieee_overflow 0
		.amdhsa_exception_fp_ieee_underflow 0
		.amdhsa_exception_fp_ieee_inexact 0
		.amdhsa_exception_int_div_zero 0
	.end_amdhsa_kernel

_Z5k_aggILb1ELi4ELb0EEvPK15HIP_vector_typeIjLj4EEPKS0_IiLj2EEPKiS8_PKfSA_PKDv8_DF16_PDF16_Pf:
	s_lshl_b32 s69, s2, 10
	v_cmp_gt_u32_e32 vcc, 16, v0
	s_and_saveexec_b64 s[4:5], vcc
	v_lshlrev_b32_e32 v1, 2, v0
	v_mov_b32_e32 v2, -1
	ds_write_b32 v1, v2 offset:17408
	s_or_b64 exec, exec, s[4:5]
	s_load_dwordx8 s[36:43], s[0:1], 0x0
	s_load_dwordx4 s[44:47], s[0:1], 0x20
	s_movk_i32 s3, 0x110
	v_cmp_gt_u32_e64 s[4:5], s3, v0
	v_lshlrev_b32_e32 v19, 4, v0
	s_and_saveexec_b64 s[6:7], s[4:5]
	s_cbranch_execz .LBB4_5
	v_mov_b32_e32 v2, 0
	v_or_b32_e32 v1, 0xffffff00, v0
	s_mov_b64 s[8:9], 0
	v_mov_b32_e32 v3, v2
	v_mov_b32_e32 v4, v2
	v_mov_b32_e32 v5, v2
	v_mov_b32_e32 v6, v19

.LBB4_5:
	s_or_b64 exec, exec, s[6:7]
	s_lshl_b32 s50, s2, 4
	s_ashr_i32 s51, s50, 31
	s_load_dwordx2 s[48:49], s[0:1], 0x40
	s_lshl_b64 s[0:1], s[50:51], 2
	s_waitcnt lgkmcnt(0)
	v_add_u32_e32 v8, s69, v0
	v_mov_b32_e32 v9, 0
	v_lshl_add_u64 v[8:9], v[8:9], 3, s[38:39]
	v_cmp_gt_u32_e64 s[6:7], 64, v0
	s_and_saveexec_b64 s[4:5], s[6:7]
	s_cbranch_execz .Lagg4_nospecb
	global_load_dwordx2 v[10:11], v[8:9], off offset:2048
.Lagg4_nospecb:
	s_mov_b64 exec, s[4:5]
	global_load_dwordx2 v[8:9], v[8:9], off
	s_add_u32 s0, s40, s0
	s_addc_u32 s1, s41, s1
	s_load_dword s33, s[0:1], 0x0
	s_min_i32 s0, s50, 0xc340
	s_ashr_i32 s1, s0, 31
	s_lshl_b64 s[0:1], s[0:1], 2
	s_add_u32 s0, s42, s0
	s_addc_u32 s1, s43, s1
	s_load_dword s51, s[0:1], 0x3c
	v_and_b32_e32 v1, 15, v0
	v_lshrrev_b32_e32 v38, 4, v0
	v_lshlrev_b32_e32 v18, 4, v1
	s_waitcnt lgkmcnt(0)
	s_cmp_ge_i32 s33, s51
	s_barrier
	s_cbranch_scc1 .Lagg4_empty
	v_mov_b32_e32 v2, 0x4400
	v_lshl_or_b32 v40, v0, 2, v2
	v_lshl_or_b32 v41, v38, 2, v2
	v_mov_b32_e32 v2, 0x2200
	v_or_b32_e32 v39, 0x3400, v18
	v_cmp_eq_u32_e64 s[0:1], 0, v1
	v_cmp_eq_u32_e64 s[2:3], 1, v38
	v_cmp_eq_u32_e64 s[4:5], 2, v38
	v_cmp_eq_u32_e64 s[6:7], 3, v38
	v_cmp_eq_u32_e64 s[8:9], 4, v38
	v_cmp_eq_u32_e64 s[10:11], 5, v38
	v_cmp_eq_u32_e64 s[12:13], 6, v38
	v_cmp_eq_u32_e64 s[14:15], 7, v38
	v_cmp_eq_u32_e64 s[16:17], 8, v38
	v_cmp_eq_u32_e64 s[18:19], 9, v38
	v_cmp_eq_u32_e64 s[20:21], 10, v38
	v_cmp_eq_u32_e64 s[22:23], 11, v38
	v_cmp_eq_u32_e64 s[24:25], 12, v38
	v_cmp_eq_u32_e64 s[26:27], 13, v38
	v_cmp_eq_u32_e64 s[28:29], 14, v38
	v_cmp_eq_u32_e64 s[30:31], 15, v38
	v_add_u32_e32 v20, s33, v0
	v_lshl_add_u32 v42, v0, 3, v2
	v_mov_b32_e32 v43, 0
	s_movk_i32 s64, 0x110
	v_mov_b32_e32 v44, -1
	s_mov_b64 s[40:41], 0x800
	s_mov_b32 s65, 0xffff0
	s_mov_b32 s66, s33
	s_branch .LBB4_8

.LBB4_44:
	s_sub_i32 s34, s51, s66
	s_min_i32 s54, s34, 0x240
	s_cmp_eq_u32 s66, s33
	s_cbranch_scc0 .Lagg4_slow
	s_cmp_eq_u32 s33, s69
	s_cbranch_scc0 .Lagg4_slow
	s_waitcnt vmcnt(0)
	v_cmp_gt_i32_e64 s[34:35], s54, v0
	s_and_saveexec_b64 s[42:43], s[34:35]
	ds_write_b64 v42, v[8:9]
	s_mov_b64 exec, s[42:43]
	v_add_u32_e32 v2, 0x100, v0
	v_cmp_gt_i32_e64 s[34:35], s54, v2
	v_cmp_gt_u32_e64 s[62:63], 64, v0
	s_and_b64 s[34:35], s[34:35], s[62:63]
	s_and_saveexec_b64 s[42:43], s[34:35]
	ds_write_b64 v42, v[10:11] offset:2048
	s_mov_b64 exec, s[42:43]
	s_cmpk_lt_i32 s54, 0x141
	s_cbranch_scc1 .LBB4_47
	v_add_u32_e32 v2, 0x140, v0
	v_cmp_gt_i32_e64 s[34:35], s54, v2
	s_and_saveexec_b64 s[42:43], s[34:35]
	s_cbranch_execz .LBB4_47
	v_add_u32_e32 v2, 0x140, v20
	v_mov_b32_e32 v3, 0
	v_lshl_add_u64 v[2:3], v[2:3], 3, s[38:39]
	global_load_dwordx2 v[6:7], v[2:3], off
	s_waitcnt vmcnt(0)
	ds_write_b64 v42, v[6:7] offset:2560
	s_branch .LBB4_47
.Lagg4_slow:
	s_waitcnt vmcnt(0)
	v_cmp_gt_i32_e64 s[34:35], s54, v0
	s_and_saveexec_b64 s[42:43], s[34:35]
	s_cbranch_execz .LBB4_47
	v_ashrrev_i32_e32 v21, 31, v20
	v_lshl_add_u64 v[2:3], v[20:21], 3, s[38:39]
	s_mov_b64 s[52:53], 0
	v_mov_b32_e32 v4, v42
	v_mov_b32_e32 v5, v0

.LBB4_101:
	s_waitcnt vmcnt(3)
	v_cvt_f32_f16_sdwa v27, v2 dst_sel:DWORD dst_unused:UNUSED_PAD src0_sel:WORD_1
	v_cvt_f32_f16_e32 v26, v2
	v_cvt_f32_f16_sdwa v29, v3 dst_sel:DWORD dst_unused:UNUSED_PAD src0_sel:WORD_1
	v_cvt_f32_f16_e32 v28, v3
	v_lshlrev_b64 v[16:17], 9, v[16:17]
	v_pk_add_f32 v[2:3], v[22:23], v[26:27]
	v_cvt_f32_f16_sdwa v23, v5 dst_sel:DWORD dst_unused:UNUSED_PAD src0_sel:WORD_1
	s_waitcnt vmcnt(0)
	v_pk_fma_f32 v[2:3], v[14:15], v[2:3], v[10:11] op_sel_hi:[0,1,1]
	v_pk_add_f32 v[10:11], v[20:21], v[28:29]
	v_cvt_f32_f16_sdwa v21, v4 dst_sel:DWORD dst_unused:UNUSED_PAD src0_sel:WORD_1
	v_cvt_f32_f16_e32 v20, v4
	v_cvt_f32_f16_e32 v22, v5
	v_lshl_add_u64 v[16:17], s[48:49], 0, v[16:17]
	v_lshlrev_b32_e32 v24, 1, v15
	v_mov_b32_e32 v25, 0
	v_lshl_add_u64 v[16:17], v[16:17], 0, v[24:25]
	v_pk_fma_f32 v[4:5], v[14:15], v[10:11], v[12:13] op_sel_hi:[0,1,1]
	v_pk_add_f32 v[10:11], v[18:19], v[20:21]
	v_pk_add_f32 v[0:1], v[0:1], v[22:23]
	v_pk_fma_f32 v[6:7], v[14:15], v[10:11], v[6:7] op_sel_hi:[0,1,1]
	v_pk_fma_f32 v[8:9], v[14:15], v[0:1], v[8:9] op_sel_hi:[0,1,1]
	v_lshlrev_b32_e32 v26, 8, v38
	v_add_u32_e32 v26, 0x2200, v26
	v_and_b32_e32 v27, 56, v15
	v_lshl_add_u32 v27, v27, 2, v26
	v_lshl_add_u32 v28, v15, 1, v26
	v_cmp_gt_u32_e64 s[2:3], 64, v15
	s_mov_b64 s[4:5], exec
	s_and_b64 exec, s[4:5], s[2:3]
	ds_write_b128 v27, v[2:5]
	ds_write_b128 v27, v[6:9] offset:16
	s_mov_b64 exec, s[4:5]
	s_waitcnt lgkmcnt(0)
	ds_read_b128 v[10:13], v28
	s_waitcnt lgkmcnt(0)
	global_store_dwordx4 v[16:17], v[10:13], off sc1
	s_andn2_b64 exec, s[4:5], s[2:3]
	ds_write_b128 v27, v[2:5]
	ds_write_b128 v27, v[6:9] offset:16
	s_mov_b64 exec, s[4:5]
	s_waitcnt lgkmcnt(0)
	ds_read_b128 v[10:13], v28
	s_waitcnt lgkmcnt(0)
	global_store_dwordx4 v[16:17], v[10:13], off offset:256 sc1
	s_endpgm
	.p2align	8

	.amdhsa_kernel _Z5k_aggILb1ELi4ELb0EEvPK15HIP_vector_typeIjLj4EEPKS0_IiLj2EEPKiS8_PKfSA_PKDv8_DF16_PDF16_Pf
		.amdhsa_group_segment_fixed_size 17472
		.amdhsa_private_segment_fixed_size 0
		.amdhsa_kernarg_size 72
		.amdhsa_user_sgpr_count 2
		.amdhsa_user_sgpr_dispatch_ptr 0
		.amdhsa_user_sgpr_queue_ptr 0
		.amdhsa_user_sgpr_kernarg_segment_ptr 1
		.amdhsa_user_sgpr_dispatch_id 0
		.amdhsa_user_sgpr_kernarg_preload_length 0
		.amdhsa_user_sgpr_kernarg_preload_offset 0
		.amdhsa_user_sgpr_private_segment_size 0
		.amdhsa_uses_dynamic_stack 0
		.amdhsa_enable_private_segment 0
		.amdhsa_system_sgpr_workgroup_id_x 1
		.amdhsa_system_sgpr_workgroup_id_y 0
		.amdhsa_system_sgpr_workgroup_id_z 0
		.amdhsa_system_sgpr_workgroup_info 0
		.amdhsa_system_vgpr_workitem_id 0
		.amdhsa_next_free_vgpr 62
		.amdhsa_next_free_sgpr 70
		.amdhsa_accum_offset 64
		.amdhsa_reserve_vcc 1
		.amdhsa_float_round_mode_32 0
		.amdhsa_float_round_mode_16_64 0
		.amdhsa_float_denorm_mode_32 3
		.amdhsa_float_denorm_mode_16_64 3
		.amdhsa_dx10_clamp 1
		.amdhsa_ieee_mode 1
		.amdhsa_fp16_overflow 0
		.amdhsa_tg_split 0
		.amdhsa_exception_fp_ieee_invalid_op 0
		.amdhsa_exception_fp_denorm_src 0
		.amdhsa_exception_fp_ieee_div_zero 0
		.amdhsa_exception_fp_ieee_overflow 0
		.amdhsa_exception_fp_ieee_underflow 0
		.amdhsa_exception_fp_ieee_inexact 0
		.amdhsa_exception_int_div_zero 0
	.end_amdhsa_kernel

amdhsa.kernels:
  - .agpr_count:     0
    .args:
      - .actual_access:  read_only
        .address_space:  global
        .offset:         0
        .size:           8
        .value_kind:     global_buffer
      - .actual_access:  read_only
        .address_space:  global
        .offset:         8
        .size:           8
        .value_kind:     global_buffer
      - .actual_access:  read_only
        .address_space:  global
        .offset:         16
        .size:           8
        .value_kind:     global_buffer
      - .actual_access:  read_only
        .address_space:  global
        .offset:         24
        .size:           8
        .value_kind:     global_buffer
      - .actual_access:  read_only
        .address_space:  global
        .offset:         32
        .size:           8
        .value_kind:     global_buffer
      - .actual_access:  write_only
        .address_space:  global
        .offset:         40
        .size:           8
        .value_kind:     global_buffer
      - .actual_access:  write_only
        .address_space:  global
        .offset:         48
        .size:           8
        .value_kind:     global_buffer
      - .actual_access:  write_only
        .address_space:  global
        .offset:         56
        .size:           8
        .value_kind:     global_buffer
      - .actual_access:  write_only
        .address_space:  global
        .offset:         64
        .size:           8
        .value_kind:     global_buffer
    .group_segment_fixed_size: 35168
    .kernarg_segment_align: 8
    .kernarg_segment_size: 72
    .language:       OpenCL C
    .language_version:
      - 2
      - 0
    .max_flat_workgroup_size: 512
    .name:           _Z6k_prepPKiPKfS2_S2_S2_PjP15HIP_vector_typeIiLj2EEPDv8_DF16_Pi
    .private_segment_fixed_size: 0
    .sgpr_count:     46
    .sgpr_spill_count: 0
    .symbol:         _Z6k_prepPKiPKfS2_S2_S2_PjP15HIP_vector_typeIiLj2EEPDv8_DF16_Pi.kd
    .uniform_work_group_size: 1
    .uses_dynamic_stack: false
    .vgpr_count:     58
    .vgpr_spill_count: 0
    .wavefront_size: 64
  - .agpr_count:     32
    .args:
      - .actual_access:  read_only
        .address_space:  global
        .offset:         0
        .size:           8
        .value_kind:     global_buffer
      - .actual_access:  read_only
        .address_space:  global
        .offset:         8
        .size:           8
        .value_kind:     global_buffer
      - .actual_access:  write_only
        .address_space:  global
        .offset:         16
        .size:           8
        .value_kind:     global_buffer
      - .actual_access:  write_only
        .address_space:  global
        .offset:         24
        .size:           8
        .value_kind:     global_buffer
      - .actual_access:  write_only
        .address_space:  global
        .offset:         32
        .size:           8
        .value_kind:     global_buffer
      - .actual_access:  write_only
        .address_space:  global
        .offset:         40
        .size:           8
        .value_kind:     global_buffer
      - .address_space:  global
        .offset:         48
        .size:           8
        .value_kind:     global_buffer
      - .actual_access:  read_only
        .address_space:  global
        .offset:         56
        .size:           8
        .value_kind:     global_buffer
      - .actual_access:  read_only
        .address_space:  global
        .offset:         64
        .size:           8
        .value_kind:     global_buffer
      - .address_space:  global
        .offset:         72
        .size:           8
        .value_kind:     global_buffer
    .group_segment_fixed_size: 38736
    .kernarg_segment_align: 8
    .kernarg_segment_size: 80
    .language:       OpenCL C
    .language_version:
      - 2
      - 0
    .max_flat_workgroup_size: 256
    .name:           _Z11k_csr_gemm1PKjPK15HIP_vector_typeIiLj2EEPS2_PiS6_PfS6_PKfPKDv8_DF16_PDF16_
    .private_segment_fixed_size: 0
    .sgpr_count:     70
    .sgpr_spill_count: 0
    .symbol:         _Z11k_csr_gemm1PKjPK15HIP_vector_typeIiLj2EEPS2_PiS6_PfS6_PKfPKDv8_DF16_PDF16_.kd
    .uniform_work_group_size: 1
    .uses_dynamic_stack: false
    .vgpr_count:     128
    .vgpr_spill_count: 0
    .wavefront_size: 64
  - .agpr_count:     0
    .args:
      - .actual_access:  read_only
        .address_space:  global
        .offset:         0
        .size:           8
        .value_kind:     global_buffer
      - .actual_access:  read_only
        .address_space:  global
        .offset:         8
        .size:           8
        .value_kind:     global_buffer
      - .actual_access:  read_only
        .address_space:  global
        .offset:         16
        .size:           8
        .value_kind:     global_buffer
      - .actual_access:  read_only
        .address_space:  global
        .offset:         24
        .size:           8
        .value_kind:     global_buffer
      - .actual_access:  read_only
        .address_space:  global
        .offset:         32
        .size:           8
        .value_kind:     global_buffer
      - .actual_access:  read_only
        .address_space:  global
        .offset:         40
        .size:           8
        .value_kind:     global_buffer
      - .actual_access:  read_only
        .address_space:  global
        .offset:         48
        .size:           8
        .value_kind:     global_buffer
      - .address_space:  global
        .offset:         56
        .size:           8
        .value_kind:     global_buffer
      - .actual_access:  read_only
        .address_space:  global
        .offset:         64
        .size:           8
        .value_kind:     global_buffer
    .group_segment_fixed_size: 17472
    .kernarg_segment_align: 8
    .kernarg_segment_size: 72
    .language:       OpenCL C
    .language_version:
      - 2
      - 0
    .max_flat_workgroup_size: 256
    .name:           _Z5k_aggILb0ELi4ELb1EEvPK15HIP_vector_typeIjLj4EEPKS0_IiLj2EEPKiS8_PKfSA_PKDv8_DF16_PDF16_Pf
    .private_segment_fixed_size: 0
    .sgpr_count:     76
    .sgpr_spill_count: 0
    .symbol:         _Z5k_aggILb0ELi4ELb1EEvPK15HIP_vector_typeIjLj4EEPKS0_IiLj2EEPKiS8_PKfSA_PKDv8_DF16_PDF16_Pf.kd
    .uniform_work_group_size: 1
    .uses_dynamic_stack: false
    .vgpr_count:     64
    .vgpr_spill_count: 0
    .wavefront_size: 64
  - .agpr_count:     0
    .args:
      - .actual_access:  read_only
        .address_space:  global
        .offset:         0
        .size:           8
        .value_kind:     global_buffer
      - .actual_access:  read_only
        .address_space:  global
        .offset:         8
        .size:           8
        .value_kind:     global_buffer
      - .actual_access:  read_only
        .address_space:  global
        .offset:         16
        .size:           8
        .value_kind:     global_buffer
      - .actual_access:  read_only
        .address_space:  global
        .offset:         24
        .size:           8
        .value_kind:     global_buffer
      - .actual_access:  read_only
        .address_space:  global
        .offset:         32
        .size:           8
        .value_kind:     global_buffer
      - .actual_access:  read_only
        .address_space:  global
        .offset:         40
        .size:           8
        .value_kind:     global_buffer
      - .actual_access:  read_only
        .address_space:  global
        .offset:         48
        .size:           8
        .value_kind:     global_buffer
      - .address_space:  global
        .offset:         56
        .size:           8
        .value_kind:     global_buffer
      - .actual_access:  read_only
        .address_space:  global
        .offset:         64
        .size:           8
        .value_kind:     global_buffer
    .group_segment_fixed_size: 17472
    .kernarg_segment_align: 8
    .kernarg_segment_size: 72
    .language:       OpenCL C
    .language_version:
      - 2
      - 0
    .max_flat_workgroup_size: 256
    .name:           _Z5k_aggILb0ELi4ELb0EEvPK15HIP_vector_typeIjLj4EEPKS0_IiLj2EEPKiS8_PKfSA_PKDv8_DF16_PDF16_Pf
    .private_segment_fixed_size: 0
    .sgpr_count:     76
    .sgpr_spill_count: 0
    .symbol:         _Z5k_aggILb0ELi4ELb0EEvPK15HIP_vector_typeIjLj4EEPKS0_IiLj2EEPKiS8_PKfSA_PKDv8_DF16_PDF16_Pf.kd
    .uniform_work_group_size: 1
    .uses_dynamic_stack: false
    .vgpr_count:     62
    .vgpr_spill_count: 0
    .wavefront_size: 64
  - .agpr_count:     0
    .args:
      - .actual_access:  read_only
        .address_space:  global
        .offset:         0
        .size:           8
        .value_kind:     global_buffer
      - .actual_access:  read_only
        .address_space:  global
        .offset:         8
        .size:           8
        .value_kind:     global_buffer
      - .actual_access:  read_only
        .address_space:  global
        .offset:         16
        .size:           8
        .value_kind:     global_buffer
      - .actual_access:  read_only
        .address_space:  global
        .offset:         24
        .size:           8
        .value_kind:     global_buffer
      - .actual_access:  read_only
        .address_space:  global
        .offset:         32
        .size:           8
        .value_kind:     global_buffer
      - .actual_access:  read_only
        .address_space:  global
        .offset:         40
        .size:           8
        .value_kind:     global_buffer
      - .actual_access:  read_only
        .address_space:  global
        .offset:         48
        .size:           8
        .value_kind:     global_buffer
      - .actual_access:  read_only
        .address_space:  global
        .offset:         56
        .size:           8
        .value_kind:     global_buffer
      - .actual_access:  write_only
        .address_space:  global
        .offset:         64
        .size:           8
        .value_kind:     global_buffer
    .group_segment_fixed_size: 17472
    .kernarg_segment_align: 8
    .kernarg_segment_size: 72
    .language:       OpenCL C
    .language_version:
      - 2
      - 0
    .max_flat_workgroup_size: 256
    .name:           _Z5k_aggILb1ELi4ELb0EEvPK15HIP_vector_typeIjLj4EEPKS0_IiLj2EEPKiS8_PKfSA_PKDv8_DF16_PDF16_Pf
    .private_segment_fixed_size: 0
    .sgpr_count:     76
    .sgpr_spill_count: 0
    .symbol:         _Z5k_aggILb1ELi4ELb0EEvPK15HIP_vector_typeIjLj4EEPKS0_IiLj2EEPKiS8_PKfSA_PKDv8_DF16_PDF16_Pf.kd
    .uniform_work_group_size: 1
    .uses_dynamic_stack: false
    .vgpr_count:     62
    .vgpr_spill_count: 0
    .wavefront_size: 64
